# grid barrier: L1 invalidate issued by wave 1 at arrival, overlapped with the barrier protocol (removed from post-release path)
# speedup vs baseline: 1.0120x; 1.0034x over previous
.LBB0_98:
	s_mov_b32 s33, s84
	s_waitcnt vmcnt(0)
	s_waitcnt lgkmcnt(0)
	s_barrier
	s_cmp_lg_u32 s86, 1
	s_cbranch_scc1 .Lxb_skipinv_0
	buffer_inv sc1
.Lxb_skipinv_0:
	s_and_saveexec_b64 s[0:1], s[76:77]
	s_cbranch_execz .LBB0_152
	s_add_i32 s2, 0, 0x25fe0
	s_waitcnt vmcnt(15)
	v_mov_b32_e32 v0, s2
	s_waitcnt vmcnt(0) expcnt(0) lgkmcnt(0)
	ds_read_b32 v2, v0
	s_add_i32 s2, 0, 0x25fe4
	v_mov_b32_e32 v0, s2
	ds_read_b32 v0, v0
	s_waitcnt lgkmcnt(1)
	v_cmp_ne_u32_e32 vcc, 0, v2
	s_cbranch_vccnz .LBB0_114
	v_readlane_b32 s2, v243, 0
	v_readlane_b32 s3, v243, 1
	s_load_dwordx2 s[6:7], s[2:3], 0x4
	s_add_u32 s2, s8, 0x1200
	s_addc_u32 s3, s9, 0
	s_add_u32 s4, s8, 0x1400
	s_addc_u32 s5, s9, 0
	s_waitcnt lgkmcnt(0)
	s_mul_i32 s46, s6, s73
	s_add_u32 s6, s8, 0x1500
	s_mul_i32 s46, s46, s7
	s_addc_u32 s7, s9, 0
	s_add_u32 s10, s8, 0x1600
	s_addc_u32 s11, s9, 0
	s_add_u32 s12, s8, 0x1700
	s_addc_u32 s13, s9, 0
	s_add_u32 s14, s8, 0x1800
	s_addc_u32 s15, s9, 0
	s_add_u32 s16, s8, 0x1900
	s_addc_u32 s17, s9, 0
	s_add_u32 s18, s8, 0x1a00
	s_addc_u32 s19, s9, 0
	s_add_u32 s20, s8, 0x1b00
	s_addc_u32 s21, s9, 0
	s_add_u32 s22, s8, 0x1c00
	s_addc_u32 s23, s9, 0
	s_add_u32 s24, s8, 0x1d00
	s_addc_u32 s25, s9, 0
	s_add_u32 s26, s8, 0x1e00
	s_addc_u32 s27, s9, 0
	s_add_u32 s28, s8, 0x1f00
	s_addc_u32 s29, s9, 0
	s_add_u32 s30, s8, 0x2000
	s_addc_u32 s31, s9, 0
	s_add_u32 s34, s8, 0x2100
	s_addc_u32 s35, s9, 0
	s_add_u32 s36, s8, 0x2200
	s_addc_u32 s37, s9, 0
	s_add_u32 s38, s8, 0x2300
	s_addc_u32 s39, s9, 0
	s_mov_b32 s47, 1
	v_mov_b32_e32 v16, 0
	s_branch .LBB0_102

.LBB0_129:
	s_or_b64 exec, exec, s[4:5]
	s_waitcnt vmcnt(0)
	s_waitcnt vmcnt(0)

.LBB0_149:
	s_or_b64 exec, exec, s[2:3]
	s_mov_b64 s[2:3], exec
	v_mbcnt_lo_u32_b32 v0, s2, 0
	v_mbcnt_hi_u32_b32 v0, s3, v0
	s_mov_b32 s7, 0
	v_cmp_eq_u32_e32 vcc, 0, v0
	s_waitcnt vmcnt(0)
	s_and_saveexec_b64 s[4:5], vcc
	s_cbranch_execz .LBB0_151
	s_add_i32 s6, s22, 0x900
	s_lshl_b64 s[6:7], s[6:7], 2
	s_add_u32 s6, s82, s6
	s_addc_u32 s7, s83, s7
	s_bcnt1_i32_b64 s2, s[2:3]
	v_mov_b32_e32 v0, 0
	v_mov_b32_e32 v1, s2
	global_atomic_add v0, v1, s[6:7]

.LBB0_152:
	s_or_b64 exec, exec, s[0:1]
	s_mov_b32 s0, s86
	s_waitcnt lgkmcnt(0)
	s_waitcnt vmcnt(0)
	s_barrier
	s_waitcnt vmcnt(15)
	v_mbcnt_lo_u32_b32 v0, -1, 0
	v_mbcnt_hi_u32_b32 v0, -1, v0
	s_mov_b32 s1, 0
	s_waitcnt vmcnt(14)
	v_lshl_add_u32 v4, s0, 6, v0
	s_add_i32 s1, s1, 0x25f98
	s_mov_b32 s0, 0
	v_mov_b32_e32 v0, s1
	ds_read_b64 v[0:1], v0
	s_add_i32 s0, s0, 0x25f28
	v_mov_b32_e32 v2, s0
	ds_read_b64 v[2:3], v2
	s_waitcnt lgkmcnt(1)
	v_readfirstlane_b32 s6, v0
	v_lshl_add_u32 v0, s74, 9, v4
	s_mov_b32 s2, 0x12000
	v_readfirstlane_b32 s7, v1
	s_waitcnt lgkmcnt(0)
	v_readfirstlane_b32 s0, v2
	v_readfirstlane_b32 s1, v3
	v_cmp_gt_i32_e32 vcc, s2, v0
	s_and_saveexec_b64 s[2:3], vcc
	s_cbranch_execz .LBB0_155
	s_add_u32 s4, s6, 0x100000
	s_addc_u32 s5, s7, 0
	s_add_u32 s6, s6, 0x400000
	s_addc_u32 s7, s7, 0
	s_lshl_b32 s12, s73, 9
	s_mov_b64 s[10:11], 0
	s_mov_b32 s13, 0x38e38e39
	s_movk_i32 s14, 0x1800
	s_movk_i32 s15, 0x6000
	s_mov_b32 s16, 0x11fff

.LBB0_155:
	s_or_b64 exec, exec, s[2:3]
	s_mov_b32 s33, s84
	s_waitcnt vmcnt(0)
	s_barrier
	s_cmp_lg_u32 s86, 1
	s_cbranch_scc1 .Lxb_skipinv_1
	buffer_inv sc1
.Lxb_skipinv_1:
	s_and_saveexec_b64 s[0:1], s[76:77]
	s_cbranch_execz .LBB0_207
	s_add_i32 s2, 0, 0x25fe0
	v_mov_b32_e32 v0, s2
	s_waitcnt vmcnt(0) expcnt(0) lgkmcnt(0)
	ds_read_b32 v2, v0
	s_add_i32 s2, 0, 0x25fe4
	v_mov_b32_e32 v0, s2
	ds_read_b32 v0, v0
	s_waitcnt lgkmcnt(1)
	v_cmp_ne_u32_e32 vcc, 0, v2
	s_cbranch_vccnz .LBB0_171
	v_readlane_b32 s2, v243, 0
	v_readlane_b32 s3, v243, 1
	s_load_dwordx2 s[6:7], s[2:3], 0x4
	s_add_u32 s2, s8, 0x1200
	s_addc_u32 s3, s9, 0
	s_add_u32 s4, s8, 0x1400
	s_addc_u32 s5, s9, 0
	s_waitcnt lgkmcnt(0)
	s_mul_i32 s46, s6, s73
	s_add_u32 s6, s8, 0x1500
	s_mul_i32 s46, s46, s7
	s_addc_u32 s7, s9, 0
	s_add_u32 s10, s8, 0x1600
	s_addc_u32 s11, s9, 0
	s_add_u32 s12, s8, 0x1700
	s_addc_u32 s13, s9, 0
	s_add_u32 s14, s8, 0x1800
	s_addc_u32 s15, s9, 0
	s_add_u32 s16, s8, 0x1900
	s_addc_u32 s17, s9, 0
	s_add_u32 s18, s8, 0x1a00
	s_addc_u32 s19, s9, 0
	s_add_u32 s20, s8, 0x1b00
	s_addc_u32 s21, s9, 0
	s_add_u32 s22, s8, 0x1c00
	s_addc_u32 s23, s9, 0
	s_add_u32 s24, s8, 0x1d00
	s_addc_u32 s25, s9, 0
	s_add_u32 s26, s8, 0x1e00
	s_addc_u32 s27, s9, 0
	s_add_u32 s28, s8, 0x1f00
	s_addc_u32 s29, s9, 0
	s_add_u32 s30, s8, 0x2000
	s_addc_u32 s31, s9, 0
	s_add_u32 s34, s8, 0x2100
	s_addc_u32 s35, s9, 0
	s_add_u32 s36, s8, 0x2200
	s_addc_u32 s37, s9, 0
	s_add_u32 s38, s8, 0x2300
	s_addc_u32 s39, s9, 0
	s_mov_b32 s47, 1
	v_mov_b32_e32 v16, 0
	s_branch .LBB0_159

.LBB0_207:
	s_or_b64 exec, exec, s[0:1]
	s_add_u32 s90, s8, 0x1200
	s_addc_u32 s91, s9, 0
	s_add_u32 s0, s8, 0x1400
	s_addc_u32 s1, s9, 0
	v_writelane_b32 v243, s0, 5
	s_mov_b32 s79, 0
	s_mov_b32 s75, s79
	v_writelane_b32 v243, s1, 6
	s_add_u32 s0, s8, 0x1500
	s_addc_u32 s1, s9, 0
	v_writelane_b32 v243, s0, 7
	v_mov_b32_e32 v65, 0
	v_mov_b32_e32 v200, 0x358637bd
	v_writelane_b32 v243, s1, 8
	s_add_u32 s0, s8, 0x1600
	s_addc_u32 s1, s9, 0
	v_writelane_b32 v243, s0, 9
	v_mov_b32_e32 v201, 1
	v_mov_b64_e32 v[196:197], 0x924
	v_writelane_b32 v243, s1, 10
	s_add_u32 s0, s8, 0x1700
	s_addc_u32 s1, s9, 0
	v_writelane_b32 v243, s0, 11
	v_mov_b64_e32 v[198:199], 0x923
	v_mov_b32_e32 v202, 0x3db504f3
	v_writelane_b32 v243, s1, 12
	s_add_u32 s0, s8, 0x1800
	s_addc_u32 s1, s9, 0
	v_writelane_b32 v243, s0, 13
	v_mov_b32_e32 v203, 0x43e00000
	v_mov_b32_e32 v204, 0x7f800000
	v_writelane_b32 v243, s1, 14
	s_add_u32 s0, s8, 0x1900
	s_addc_u32 s1, s9, 0
	v_writelane_b32 v243, s0, 15
	v_mov_b32_e32 v205, 0x2400
	v_mov_b32_e32 v206, 0x42f00000
	v_writelane_b32 v243, s1, 16
	s_add_u32 s0, s8, 0x1a00
	s_addc_u32 s1, s9, 0
	v_writelane_b32 v243, s0, 17
	v_mov_b32_e32 v207, 0xc2f00000
	v_mov_b32_e32 v208, 0x208000
	v_writelane_b32 v243, s1, 18
	s_add_u32 s0, s8, 0x1b00
	s_addc_u32 s1, s9, 0
	v_writelane_b32 v243, s0, 19
	v_mov_b32_e32 v209, 0x8200
	v_mov_b32_e32 v210, 0x10000
	v_writelane_b32 v243, s1, 20
	s_add_u32 s0, s8, 0x1c00
	s_addc_u32 s1, s9, 0
	v_writelane_b32 v243, s0, 21
	s_movk_i32 s87, 0x100
	s_mov_b32 s95, 0xffff0000
	v_writelane_b32 v243, s1, 22
	s_add_u32 s0, s8, 0x1d00
	s_addc_u32 s1, s9, 0
	v_writelane_b32 v243, s0, 23
	s_mov_b32 s72, 0xc3e00000
	s_mov_b32 s81, 0xc2f00000
	v_writelane_b32 v243, s1, 24
	s_add_u32 s0, s8, 0x1e00
	s_addc_u32 s1, s9, 0
	v_writelane_b32 v243, s0, 25
	s_mov_b64 s[68:69], 0x80
	s_mov_b32 s94, 0x3fb8aa3b
	v_writelane_b32 v243, s1, 26
	s_add_u32 s0, s8, 0x1f00
	s_addc_u32 s1, s9, 0
	v_writelane_b32 v243, s0, 27
	s_waitcnt lgkmcnt(0)
	s_waitcnt vmcnt(0)
	s_barrier
	v_writelane_b32 v243, s1, 28
	s_add_u32 s0, s8, 0x2000
	s_addc_u32 s1, s9, 0
	v_writelane_b32 v243, s0, 29
	s_nop 1
	v_writelane_b32 v243, s1, 30
	s_add_u32 s0, s8, 0x2100
	s_addc_u32 s1, s9, 0
	v_writelane_b32 v243, s0, 31
	s_nop 1
	v_writelane_b32 v243, s1, 32
	s_add_u32 s0, s8, 0x2200
	s_addc_u32 s1, s9, 0
	v_writelane_b32 v243, s0, 33
	s_nop 1
	v_writelane_b32 v243, s1, 34
	s_add_u32 s0, s8, 0x2300
	s_addc_u32 s1, s9, 0
	v_writelane_b32 v243, s0, 35
	s_nop 1
	v_writelane_b32 v243, s1, 36
	s_add_u32 s0, s8, 0x4400
	s_addc_u32 s1, s9, 0
	v_writelane_b32 v243, s0, 37
	s_nop 1
	v_writelane_b32 v243, s1, 38
	s_add_u32 s0, s8, 0x4500
	s_addc_u32 s1, s9, 0
	v_writelane_b32 v243, s0, 39
	s_cmpk_lt_i32 s74, 0x924
	s_nop 0
	v_writelane_b32 v243, s1, 40
	s_cselect_b64 s[0:1], -1, 0
	v_writelane_b32 v243, s0, 41
	s_ashr_i32 s2, s74, 31
	s_nop 0
	v_writelane_b32 v243, s1, 42
	s_lshr_b32 s0, s2, 29
	s_add_i32 s0, s74, s0
	s_ashr_i32 s3, s0, 3
	s_and_b32 s0, s0, -8
	s_sub_i32 s4, s74, s0
	s_mul_i32 s0, s4, 0x124
	s_add_i32 s5, s0, 4
	s_ashr_i32 s0, s73, 31
	v_writelane_b32 v243, s0, 43
	s_cmp_gt_i32 s74, 35
	v_readlane_b32 s10, v243, 3
	s_cselect_b64 s[0:1], -1, 0
	v_readlane_b32 s11, v243, 4
	s_and_b64 s[0:1], s[0:1], s[10:11]
	v_writelane_b32 v243, s0, 44
	s_nop 1
	v_writelane_b32 v243, s1, 45
	s_lshl_b32 s0, s74, 5
	s_addk_i32 s0, 0x20e0
	v_writelane_b32 v243, s0, 46
	s_lshl_b64 s[0:1], s[74:75], 17
	v_writelane_b32 v243, s0, 47
	s_cmp_lt_i32 s73, 32
	s_nop 0
	v_writelane_b32 v243, s1, 48
	s_cselect_b64 s[0:1], -1, 0
	v_writelane_b32 v243, s0, 49
	s_cmp_gt_i32 s74, 15
	s_nop 0
	v_writelane_b32 v243, s1, 50
	s_cselect_b64 s[0:1], -1, 0
	v_writelane_b32 v243, s0, 51
	s_cmp_lt_i32 s74, 16
	s_nop 0
	v_writelane_b32 v243, s1, 52
	s_cselect_b64 s[0:1], -1, 0
	v_writelane_b32 v243, s0, 53
	s_bitcmp1_b32 s74, 2
	s_nop 0
	v_writelane_b32 v243, s1, 54
	s_cselect_b64 s[0:1], -1, 0
	v_writelane_b32 v243, s0, 55
	s_lshr_b32 s6, s74, 3
	s_nop 0
	v_writelane_b32 v243, s1, 56
	s_and_b32 s0, s74, 3
	s_lshl_b32 s7, s0, 7
	v_writelane_b32 v243, s0, 57
	s_or_b32 s0, s7, 0xa00
	v_writelane_b32 v243, s0, 58
	s_or_b32 s0, s7, 0xe00
	v_writelane_b32 v243, s0, 59
	s_or_b32 s1, s7, 0xc00
	s_lshl_b32 s0, s74, 7
	v_writelane_b32 v243, s1, 60
	s_lshl_b32 s1, s74, 1
	s_and_b32 s8, s0, 0x380
	v_writelane_b32 v243, s1, 61
	s_and_b32 s0, s0, 0x180
	v_writelane_b32 v243, s0, 62
	s_add_i32 s0, s73, -16
	s_cmpk_lt_i32 s74, 0x800
	v_writelane_b32 v243, s0, 63
	s_cselect_b64 s[0:1], -1, 0
	v_writelane_b32 v242, s0, 0
	s_cmpk_lt_i32 s74, 0x100
	s_nop 0
	v_writelane_b32 v242, s1, 1
	s_cselect_b64 s[0:1], -1, 0
	v_writelane_b32 v242, s0, 2
	s_cmpk_lt_i32 s74, 0x200
	s_nop 0
	v_writelane_b32 v242, s1, 3
	s_cselect_b64 s[0:1], -1, 0
	s_ashr_i32 s9, s71, 2
	s_and_b32 s12, s71, 3
	v_writelane_b32 v242, s0, 4
	s_cmp_gt_i32 s9, 63
	s_nop 0
	v_writelane_b32 v242, s1, 5
	s_cselect_b64 s[0:1], -1, 0
	s_cmp_lg_u64 s[0:1], 0
	v_writelane_b32 v242, s9, 6
	s_addc_u32 s0, s9, 1
	v_writelane_b32 v242, s0, 7
	s_lshl_b32 s0, s12, 19
	v_writelane_b32 v242, s12, 8
	s_cmp_gt_i32 s71, 7
	v_writelane_b32 v242, s0, 9
	s_cselect_b64 s[0:1], -1, 0
	v_writelane_b32 v242, s0, 10
	s_lshl_b32 s9, s71, 5
	s_nop 0
	v_writelane_b32 v242, s1, 11
	s_add_i32 s0, s9, 0x3fe0
	s_cmp_gt_i32 s74, 3
	v_writelane_b32 v242, s0, 12
	s_cselect_b64 s[0:1], -1, 0
	v_writelane_b32 v242, s0, 13
	s_nop 1
	v_writelane_b32 v242, s1, 14
	v_readlane_b32 s0, v243, 2
	s_addk_i32 s0, 0x5fc0
	s_cmp_gt_i32 s74, 63
	v_writelane_b32 v242, s0, 15
	s_cselect_b64 s[0:1], -1, 0
	s_and_b64 s[0:1], s[0:1], s[10:11]
	v_writelane_b32 v242, s0, 16
	s_nop 1
	v_writelane_b32 v242, s1, 17
	s_lshl_b32 s0, s74, 4
	s_addk_i32 s0, 0x3ce0
	v_writelane_b32 v242, s0, 18
	s_and_b32 s0, s71, 15
	s_cmp_gt_i32 s71, 63
	v_writelane_b32 v242, s0, 19
	s_cselect_b64 s[0:1], -1, 0
	v_writelane_b32 v242, s0, 20
	s_nop 1
	v_writelane_b32 v242, s1, 21
	s_add_i32 s0, s9, 0x6bc0
	s_cmp_lt_i32 s4, 4
	s_mulk_i32 s4, 0x125
	v_writelane_b32 v242, s0, 22
	s_cselect_b32 s0, s4, s5
	s_add_i32 s0, s0, s3
	s_mul_hi_i32 s1, s0, 0x38e38e39
	s_lshr_b32 s3, s1, 31
	s_ashr_i32 s1, s1, 5
	s_add_i32 s1, s1, s3
	s_mul_i32 s3, s1, 0x90
	s_lshl_b32 s4, s1, 3
	s_sub_i32 s3, s0, s3
	s_sub_i32 s0, 0x82, s4
	s_min_u32 s5, s0, 8
	v_cvt_f32_ubyte0_e32 v1, s5
	v_cvt_f32_i32_e32 v0, s3
	v_rcp_iflag_f32_e32 v2, v1
	s_ashr_i32 s0, s3, 30
	s_or_b32 s9, s0, 1
	v_writelane_b32 v242, s2, 23
	v_mul_f32_e32 v2, v0, v2
	v_trunc_f32_e32 v2, v2
	v_fma_f32 v0, -v2, v1, v0
	v_cmp_ge_f32_e64 s[0:1], |v0|, v1
	v_cvt_i32_f32_e32 v0, v2
	s_and_b64 s[0:1], s[0:1], exec
	s_cselect_b32 s0, s9, 0
	s_mul_i32 s2, s6, 0x4100
	v_readfirstlane_b32 s1, v0
	s_add_i32 s0, s1, s0
	s_mul_i32 s1, s0, s5
	s_sub_i32 s1, s3, s1
	s_sext_i32_i16 s1, s1
	v_writelane_b32 v242, s2, 24
	s_add_i32 s2, s4, s1
	s_sext_i32_i16 s1, s0
	v_writelane_b32 v242, s1, 25
	s_bfe_i64 s[0:1], s[0:1], 0x100000
	s_lshl_b64 s[0:1], s[0:1], 19
	v_writelane_b32 v242, s0, 26
	s_ashr_i32 s3, s2, 31
	s_mov_b32 s6, s79
	v_writelane_b32 v242, s1, 27
	s_lshl_b32 s0, s7, 1
	v_writelane_b32 v242, s0, 28
	s_lshl_b32 s0, s8, 1
	v_writelane_b32 v242, s0, 29
	s_ashr_i32 s0, s71, 31
	v_writelane_b32 v242, s0, 30
	s_abs_i32 s0, s71
	v_writelane_b32 v242, s0, 31
	s_add_i32 s0, 0, 0x25fe0
	v_writelane_b32 v242, s0, 32
	s_add_i32 s0, 0, 0x25fe4
	v_writelane_b32 v242, s0, 33
	s_mov_b32 s0, s2
	v_writelane_b32 v242, s0, 34
	s_nop 1
	v_writelane_b32 v242, s1, 35
	s_lshl_b64 s[0:1], s[2:3], 19
	v_writelane_b32 v242, s0, 36
	s_nop 1
	v_writelane_b32 v242, s1, 37
	s_mov_b32 s0, s74
	v_writelane_b32 v242, s0, 38
	s_nop 1
	v_writelane_b32 v242, s1, 39
	v_writelane_b32 v242, s73, 40
	v_writelane_b32 v242, s71, 41
	v_writelane_b32 v242, s76, 42
	s_nop 1
	v_writelane_b32 v242, s77, 43
	v_writelane_b32 v242, s80, 44
	v_writelane_b32 v242, s82, 45
	s_nop 1
	v_writelane_b32 v242, s83, 46
	v_writelane_b32 v242, s84, 47
	v_writelane_b32 v242, s86, 48
	v_writelane_b32 v242, s90, 49
	s_nop 1
	v_writelane_b32 v242, s91, 50
	s_branch .LBB0_210

.LBB0_209:
	s_or_b64 exec, exec, s[0:1]
	v_readlane_b32 s6, v242, 55
	s_add_i32 s6, s6, 1
	s_cmp_eq_u32 s6, 4
	s_waitcnt lgkmcnt(0)
	s_waitcnt vmcnt(0)
	s_barrier
	v_readlane_b32 s7, v242, 56
	s_cbranch_scc0 .LBB0_210
	s_getpc_b64 s[98:99]

.LBB0_245:
	s_mov_b32 s2, s84
	s_waitcnt vmcnt(0)
	s_waitcnt lgkmcnt(0)
	s_barrier
	v_readlane_b32 s100, v242, 48
	s_nop 3
	s_cmp_lg_u32 s100, 1
	s_cbranch_scc1 .Lxb_skipinv_2
	buffer_inv sc1
.Lxb_skipinv_2:
	s_and_saveexec_b64 s[0:1], s[76:77]
	s_cbranch_execz .LBB0_297
	v_readlane_b32 s3, v242, 32
	s_waitcnt vmcnt(0) expcnt(0) lgkmcnt(0)
	s_nop 0
	v_mov_b32_e32 v0, s3
	ds_read_b32 v2, v0
	v_readlane_b32 s3, v242, 33
	s_waitcnt lgkmcnt(0)
	v_cmp_ne_u32_e32 vcc, 0, v2
	v_mov_b32_e32 v0, s3
	ds_read_b32 v0, v0
	s_cbranch_vccnz .LBB0_261
	v_readlane_b32 s6, v243, 0
	v_readlane_b32 s7, v243, 1
	s_load_dwordx2 s[4:5], s[6:7], 0x4
	s_mov_b32 s10, 1
	s_waitcnt lgkmcnt(0)
	s_mul_i32 s3, s4, s73
	s_mul_i32 s3, s3, s5
	s_branch .LBB0_249

.LBB0_276:
	s_or_b64 exec, exec, s[6:7]
	s_waitcnt vmcnt(0)
	s_waitcnt vmcnt(0)

.LBB0_294:
	s_or_b64 exec, exec, s[4:5]
	s_mov_b64 s[4:5], exec
	v_mbcnt_lo_u32_b32 v0, s4, 0
	v_mbcnt_hi_u32_b32 v0, s5, v0
	v_cmp_eq_u32_e32 vcc, 0, v0
	s_waitcnt vmcnt(0)
	s_and_saveexec_b64 s[6:7], vcc
	s_cbranch_execz .LBB0_296
	s_add_i32 s78, s2, 0x900
	s_lshl_b64 s[2:3], s[78:79], 2
	s_add_u32 s2, s82, s2
	s_addc_u32 s3, s83, s3
	s_bcnt1_i32_b64 s4, s[4:5]
	v_mov_b32_e32 v0, s4
	global_atomic_add v65, v0, s[2:3]

.LBB0_297:
	s_or_b64 exec, exec, s[0:1]
	v_readlane_b32 s0, v242, 51
	s_add_u32 s2, s0, 0x3b600000
	v_readlane_b32 s0, v242, 52
	s_addc_u32 s3, s0, 0
	v_writelane_b32 v242, s2, 53
	s_mov_b32 s0, s86
	s_waitcnt lgkmcnt(0)
	v_writelane_b32 v242, s3, 54
	s_mov_b32 s2, s79
	s_waitcnt vmcnt(0)
	s_barrier
	v_mbcnt_lo_u32_b32 v0, -1, 0
	v_mbcnt_hi_u32_b32 v0, -1, v0
	s_mov_b32 s4, s28
	s_waitcnt vmcnt(12)
	v_lshl_add_u32 v14, s0, 6, v0
	v_readlane_b32 s0, v243, 41
	s_mov_b32 s5, s79
	v_readlane_b32 s1, v243, 42
	s_andn2_b64 vcc, exec, s[0:1]
	v_readfirstlane_b32 s3, v14
	v_writelane_b32 v242, s4, 55
	s_nop 1
	v_writelane_b32 v242, s5, 56
	s_cbranch_vccnz .LBB0_333
	v_lshlrev_b32_e32 v0, 4, v14
	v_add_u32_e32 v1, 0x2000, v0
	v_ashrrev_i32_e32 v2, 31, v1
	v_lshrrev_b32_e32 v2, 22, v2
	v_add_u32_e32 v2, v1, v2
	v_ashrrev_i32_e32 v8, 10, v2
	v_mul_i32_i24_e32 v2, 0x400, v8
	v_sub_u32_e32 v1, v1, v2
	v_lshrrev_b32_e32 v2, 4, v1
	v_bitop3_b32 v1, v2, v1, 32 bitop3:0x6c
	v_ashrrev_i32_e32 v2, 31, v1
	s_mul_hi_u32 s0, s4, 0x900000
	s_mul_i32 s1, s4, 0x900000
	v_readlane_b32 s4, v242, 51
	v_lshrrev_b32_e32 v2, 26, v2
	s_add_u32 s1, s4, s1
	v_readlane_b32 s4, v242, 52
	v_add_u32_e32 v2, v1, v2
	v_lshlrev_b32_e32 v3, 3, v8
	s_addc_u32 s0, s4, s0
	v_ashrrev_i32_e32 v9, 6, v2
	v_and_b32_e32 v3, -16, v3
	s_add_u32 s30, s1, 0x800000
	v_add_u32_e32 v3, v9, v3
	s_addc_u32 s31, s0, 0
	v_and_b32_e32 v4, 3, v9
	s_mov_b32 s0, 0x1fffe0
	v_lshrrev_b32_e32 v5, 2, v3
	v_lshlrev_b32_e32 v6, 1, v3
	v_and_b32_e32 v2, 0xc0, v2
	v_and_or_b32 v4, v3, s0, v4
	v_and_b32_e32 v5, 4, v5
	v_and_b32_e32 v6, 24, v6
	v_sub_u32_e32 v1, v1, v2
	v_or3_b32 v4, v4, v5, v6
	v_lshlrev_b32_e32 v5, 5, v8
	v_ashrrev_i16_sdwa v1, v201, sext(v1) dst_sel:DWORD dst_unused:UNUSED_PAD src0_sel:DWORD src1_sel:BYTE_0
	v_and_b32_e32 v5, 32, v5
	v_bfe_i32 v10, v1, 0, 16
	v_add_lshl_u32 v1, v5, v10, 1
	v_lshl_add_u32 v146, v4, 11, v1
	v_lshl_add_u32 v148, v3, 11, v1
	v_bfe_i32 v1, v14, 27, 1
	v_lshrrev_b32_e32 v1, 22, v1
	v_add_u32_e32 v1, v0, v1
	v_and_b32_e32 v1, 0xfffffc00, v1
	v_sub_u32_e32 v0, v0, v1
	v_lshrrev_b32_e32 v1, 4, v0
	v_bitop3_b32 v1, v1, v0, 32 bitop3:0x6c
	v_ashrrev_i32_e32 v0, 31, v0
	v_lshrrev_b32_e32 v0, 26, v0
	v_add_u32_e32 v0, v1, v0
	v_ashrrev_i32_e32 v11, 6, v0
	v_ashrrev_i32_e32 v0, 31, v14
	v_lshrrev_b32_e32 v0, 26, v0
	v_add_u32_e32 v0, v14, v0
	v_ashrrev_i32_e32 v12, 6, v0
	v_lshlrev_b32_e32 v0, 3, v12
	v_and_b32_e32 v0, -16, v0
	v_add_u32_e32 v0, v11, v0
	s_ashr_i32 s6, s3, 6
	v_and_b32_e32 v2, 3, v11
	v_lshrrev_b32_e32 v3, 2, v0
	v_lshlrev_b32_e32 v4, 1, v0
	s_ashr_i32 s5, s3, 8
	s_lshl_b32 s4, s6, 10
	v_and_or_b32 v2, v0, s0, v2
	v_and_b32_e32 v3, 4, v3
	v_and_b32_e32 v4, 24, v4
	v_readlane_b32 s0, v242, 26
	v_or3_b32 v2, v2, v3, v4
	v_mul_i32_i24_e32 v4, 64, v11
	v_readlane_b32 s1, v242, 27
	s_add_u32 s26, s30, s0
	v_sub_u32_e32 v1, v1, v4
	s_addc_u32 s27, s31, s1
	s_add_i32 s34, s2, 0x10000
	v_lshlrev_b32_e32 v3, 5, v12
	v_ashrrev_i16_sdwa v1, v201, sext(v1) dst_sel:DWORD dst_unused:UNUSED_PAD src0_sel:DWORD src1_sel:BYTE_0
	s_add_i32 s35, s34, s4
	v_and_b32_e32 v3, 32, v3
	v_bfe_i32 v13, v1, 0, 16
	s_add_i32 s36, s35, 0x2000
	v_add_lshl_u32 v1, v3, v13, 1
	s_add_u32 s0, s26, 0x40000
	v_lshl_add_u32 v150, v2, 11, v1
	s_mov_b32 m0, s35
	s_addc_u32 s1, s27, 0
	s_add_i32 s37, s2, 0x14000
	global_load_lds_dwordx4 v150, s[26:27]
	s_mov_b32 m0, s36
	s_add_i32 s38, s37, s4
	global_load_lds_dwordx4 v146, s[26:27]
	s_mov_b32 m0, s38
	s_add_i32 s39, s38, 0x2000
	global_load_lds_dwordx4 v150, s[0:1]
	s_mov_b32 m0, s39
	v_readlane_b32 s8, v242, 53
	global_load_lds_dwordx4 v146, s[0:1]
	v_readlane_b32 s0, v242, 36
	v_readlane_b32 s1, v242, 37
	v_readlane_b32 s9, v242, 54
	s_add_u32 s24, s8, s0
	s_addc_u32 s25, s9, s1
	s_add_i32 s40, s2, s4
	s_add_i32 s41, s40, 0x2000
	v_lshl_add_u32 v152, v0, 11, v1
	s_mov_b32 m0, s40
	s_add_u32 s0, s24, 0x40000
	global_load_lds_dwordx4 v152, s[24:25]
	s_mov_b32 m0, s41
	s_addc_u32 s1, s25, 0
	s_add_i32 s42, s40, 0x4000
	global_load_lds_dwordx4 v148, s[24:25]
	s_mov_b32 m0, s42
	s_add_i32 s43, s40, 0x6000
	global_load_lds_dwordx4 v152, s[0:1]
	s_mov_b32 m0, s43
	v_mov_b32_e32 v151, v65
	global_load_lds_dwordx4 v148, s[0:1]
	v_mov_b32_e32 v147, v65
	v_mov_b32_e32 v153, v65
	v_mov_b32_e32 v149, v65
	s_cmp_eq_u32 s5, 1
	v_lshl_add_u64 v[6:7], s[26:27], 0, v[150:151]
	v_lshl_add_u64 v[4:5], s[26:27], 0, v[146:147]
	v_lshl_add_u64 v[0:1], s[24:25], 0, v[152:153]
	s_cselect_b64 s[0:1], -1, 0
	s_cmp_lg_u32 s5, 1
	v_lshl_add_u64 v[2:3], s[24:25], 0, v[148:149]
	s_cbranch_scc1 .LBB0_300
	s_barrier

.LBB0_358:
	s_mov_b32 s2, s84
	s_waitcnt vmcnt(0)
	s_waitcnt vmcnt(0)
	s_barrier
	v_readlane_b32 s100, v242, 48
	s_nop 3
	s_cmp_lg_u32 s100, 1
	s_cbranch_scc1 .Lxb_skipinv_3
	buffer_inv sc1

.LBB0_410:
	s_or_b64 exec, exec, s[0:1]
	s_mov_b32 s0, s86
	s_waitcnt lgkmcnt(0)
	s_waitcnt vmcnt(0)
	s_barrier
	v_readlane_b32 s4, v242, 55
	v_mbcnt_lo_u32_b32 v0, -1, 0
	v_mbcnt_hi_u32_b32 v0, -1, v0
	s_mov_b32 s65, s79
	v_lshl_add_u32 v122, s0, 6, v0
	s_mov_b32 s0, s79
	s_cmp_eq_u32 s4, 3
	s_cselect_b64 s[6:7], -1, 0
	s_add_i32 s0, s0, 0x25f98
	v_mov_b32_e32 v0, s0
	ds_read_b64 v[0:1], v0
	v_readfirstlane_b32 s70, v122
	s_ashr_i32 s93, s70, 6
	v_readlane_b32 s5, v242, 56
	v_and_b32_e32 v160, 63, v122
	s_waitcnt lgkmcnt(0)
	v_readfirstlane_b32 s0, v0
	v_readfirstlane_b32 s1, v1
	s_add_u32 s8, s0, 0x43800000
	s_addc_u32 s9, s1, 0
	s_add_u32 s2, s0, 0x65800000
	v_writelane_b32 v242, s2, 58
	s_addc_u32 s2, s1, 0
	v_writelane_b32 v242, s2, 60
	s_add_u32 s2, s0, 0x6da00000
	s_addc_u32 s3, s1, 0
	v_writelane_b32 v242, s2, 62
	s_nop 1
	v_writelane_b32 v242, s3, 63
	s_add_u32 s2, s0, 0x3f700000
	v_writelane_b32 v241, s2, 0
	s_addc_u32 s2, s1, 0
	v_writelane_b32 v241, s2, 2
	v_readlane_b32 s2, v243, 47
	v_readlane_b32 s3, v243, 48
	s_add_u32 s0, s0, s2
	s_addc_u32 s1, s1, s3
	s_add_u32 s30, s0, 0x6dc00000
	s_mov_b32 s0, s79
	s_addc_u32 s31, s1, 0
	s_add_i32 s0, s0, 0x25f60
	v_mov_b32_e32 v0, s0
	ds_read_b64 v[0:1], v0
	s_lshl_b32 s78, s4, 3
	s_lshl_b64 s[2:3], s[78:79], 2
	s_waitcnt lgkmcnt(0)
	v_readfirstlane_b32 s0, v0
	v_readfirstlane_b32 s1, v1
	s_add_u32 s0, s0, s2
	v_writelane_b32 v241, s2, 4
	s_addc_u32 s1, s1, s3
	s_lshl_b32 s78, s4, 7
	v_writelane_b32 v241, s3, 5
	v_writelane_b32 v241, s0, 6
	s_lshl_b64 s[2:3], s[78:79], 2
	s_mov_b64 s[4:5], -1
	v_writelane_b32 v241, s1, 7
	s_mov_b32 s0, s79
	s_add_i32 s0, s0, 0x25f58
	v_mov_b32_e32 v0, s0
	ds_read_b64 v[0:1], v0
	s_waitcnt lgkmcnt(0)
	v_readfirstlane_b32 s0, v0
	s_add_u32 s55, s0, s2
	v_writelane_b32 v241, s2, 8
	v_readfirstlane_b32 s1, v1
	s_addc_u32 s56, s1, s3
	v_writelane_b32 v241, s3, 9
	v_writelane_b32 v241, s6, 10
	v_readlane_b32 s0, v243, 49
	v_readlane_b32 s1, v243, 50
	v_writelane_b32 v241, s7, 11
	v_writelane_b32 v241, s88, 12
	s_or_b64 s[0:1], s[0:1], s[6:7]
	s_andn2_b64 vcc, exec, s[0:1]
	v_writelane_b32 v241, s89, 13
	v_writelane_b32 v241, s8, 14
	s_nop 1
	v_writelane_b32 v241, s9, 15
	v_writelane_b32 v241, s75, 16
	s_cbranch_vccz .LBB0_497
	v_readlane_b32 s0, v243, 53
	v_readlane_b32 s1, v243, 54
	s_and_b64 vcc, exec, s[0:1]
	v_lshlrev_b32_e32 v64, 1, v160
	s_cbranch_vccz .LBB0_435
	s_lshl_b32 s88, s93, 3
	v_readlane_b32 s0, v243, 55
	s_bfe_u32 s48, s70, 0x20006
	v_lshlrev_b32_e32 v66, 2, v160
	v_mov_b32_e32 v67, v65
	v_readlane_b32 s1, v243, 56
	v_writelane_b32 v241, s88, 25
	s_ashr_i32 s33, s70, 8
	v_lshl_add_u64 v[68:69], s[8:9], 0, v[66:67]
	s_lshl_b32 s64, s48, 4
	s_andn2_b64 vcc, exec, s[0:1]
	v_lshlrev_b32_e32 v56, 2, v64
	v_writelane_b32 v241, s55, 55
	v_writelane_b32 v241, s56, 59
	s_cbranch_vccnz .LBB0_437
	s_lshl_b32 s0, s93, 1
	s_and_b32 s0, s0, 0x3ffffc
	v_lshrrev_b32_e32 v0, 4, v160
	v_lshlrev_b32_e32 v148, 2, v160
	v_or_b32_e32 v0, s0, v0
	s_lshl_b32 s0, s93, 5
	v_lshlrev_b32_e32 v0, 10, v0
	v_and_b32_e32 v1, 60, v148
	s_and_b32 s1, s0, 32
	v_bitop3_b32 v0, v0, s1, v1 bitop3:0xf6
	s_lshl_b32 s1, s93, 9
	v_writelane_b32 v241, s1, 41
	s_and_b32 s1, s1, 0x200
	s_or_b32 s61, s88, 1
	v_or_b32_e32 v1, s1, v0
	s_lshl_b32 s1, s61, 6
	s_and_b32 s1, s1, 0x240
	s_or_b32 s57, s88, 2
	v_or_b32_e32 v2, s1, v0
	s_lshl_b32 s1, s57, 6
	s_and_b32 s1, s1, 0x280
	s_or_b32 s60, s88, 3
	v_or_b32_e32 v3, s1, v0
	s_lshl_b32 s1, s60, 6
	s_and_b32 s1, s1, 0x2c0
	v_or_b32_e32 v4, s1, v0
	s_or_b32 s1, s88, 4
	s_sub_i32 s2, 63, s1
	s_mov_b32 s96, s1
	s_lshl_b32 s1, s1, 6
	s_and_b32 s1, s1, 0x300
	v_or_b32_e32 v5, s1, v0
	s_or_b32 s1, s88, 5
	s_mov_b32 s62, s2
	v_cvt_f32_i32_e32 v153, s2
	s_sub_i32 s2, 63, s1
	s_mov_b32 s72, s1
	s_lshl_b32 s1, s1, 6
	s_and_b32 s1, s1, 0x340
	v_or_b32_e32 v6, s1, v0
	s_or_b32 s1, s88, 6
	v_writelane_b32 v241, s2, 45
	v_cvt_f32_i32_e32 v154, s2
	s_sub_i32 s2, 63, s1
	v_writelane_b32 v241, s2, 23
	v_writelane_b32 v241, s1, 19
	s_lshl_b32 s1, s1, 6
	s_and_b32 s1, s1, 0x380
	v_or_b32_e32 v7, s1, v0
	s_or_b32 s1, s88, 7
	v_cvt_f32_i32_e32 v155, s2
	s_sub_i32 s2, 63, s1
	v_writelane_b32 v241, s2, 27
	v_writelane_b32 v241, s1, 21
	s_lshl_b32 s1, s1, 6
	s_and_b32 s1, s1, 0x3c0
	s_sub_i32 s58, 63, s88
	s_sub_i32 s63, 63, s61
	s_sub_i32 s59, 63, s57
	s_sub_i32 s66, 63, s60
	v_or_b32_e32 v0, s1, v0
	s_lshl_b32 s4, s93, 4
	v_readlane_b32 s1, v242, 28
	v_ashrrev_i32_e32 v123, 31, v122
	s_add_u32 s6, s8, s1
	v_lshlrev_b64 v[124:125], 3, v[122:123]
	s_mov_b64 s[10:11], 0x1000
	s_addc_u32 s7, s9, 0
	s_and_b32 s5, s93, -4
	v_lshl_add_u64 v[126:127], v[124:125], 0, s[10:11]
	s_mov_b64 s[10:11], 0x2000
	s_add_i32 s1, s65, 0x12000
	s_lshl_b32 s8, s5, 12
	v_lshl_add_u64 v[128:129], v[124:125], 0, s[10:11]
	s_mov_b64 s[10:11], 0x3000
	v_lshrrev_b32_e32 v8, 2, v122
	s_lshl_b32 s3, s48, 11
	s_add_i32 s22, s1, s8
	s_lshl_b32 s8, s5, 11
	v_lshl_add_u64 v[130:131], v[124:125], 0, s[10:11]
	s_mov_b64 s[10:11], 0x4000
	v_cvt_f32_i32_e32 v156, s2
	v_and_b32_e32 v8, 14, v8
	s_lshl_b32 s2, s48, 12
	s_add_i32 s3, s65, s3
	s_add_i32 s23, s65, s8
	s_lshl_b32 s8, s93, 11
	s_lshl_b32 s26, s33, 6
	v_lshl_add_u64 v[132:133], v[124:125], 0, s[10:11]
	s_mov_b64 s[10:11], 0x5000
	v_lshlrev_b32_e32 v161, 3, v160
	v_add_lshl_u32 v158, v8, s33, 10
	v_lshlrev_b32_e32 v8, 7, v160
	s_lshl_b32 s16, s33, 1
	s_add_i32 s2, s65, s2
	s_add_i32 s3, s3, 0x10000
	s_add_i32 s24, s65, s8
	s_add_i32 s25, s65, 0x1b600
	s_xor_b32 s27, s26, 64
	s_lshl_b32 s20, s48, 1
	v_lshl_add_u64 v[134:135], v[124:125], 0, s[10:11]
	s_mov_b64 s[10:11], 0x6000
	v_and_b32_e32 v159, 0x380, v8
	v_and_b32_e32 v8, 32, v161
	s_cmp_lt_u32 s70, 64
	v_lshl_add_u64 v[136:137], v[124:125], 0, s[10:11]
	s_mov_b64 s[10:11], 0x7000
	v_bitop3_b32 v67, s4, v8, 48 bitop3:0x6c
	v_writelane_b32 v241, s8, 49
	s_cselect_b64 s[8:9], -1, 0
	v_lshl_add_u64 v[138:139], v[124:125], 0, s[10:11]
	s_lshl_b32 s10, s5, 4
	s_or_b32 s12, s4, 48
	s_lshl_b32 s28, s48, 8
	s_lshl_b32 s4, s33, 7
	s_ashr_i32 s11, s10, 31
	s_ashr_i32 s13, s12, 31
	s_add_i32 s28, s28, s4
	s_cmp_le_i32 s16, s48
	s_cselect_b64 s[14:15], -1, 0
	s_lshl_b32 s42, s33, 13
	s_lshl_b32 s43, s33, 5
	s_lshl_b32 s44, s33, 10
	s_or_b32 s4, s16, 1
	s_cmp_lt_i32 s16, s48
	s_cselect_b64 s[16:17], -1, 0
	s_lshl_b32 s45, s4, 12
	s_lshl_b32 s46, s4, 4
	s_lshl_b32 s47, s4, 5
	v_readlane_b32 s4, v242, 29
	v_readlane_b32 s5, v241, 0
	v_cvt_f32_i32_e32 v149, s58
	v_cvt_f32_i32_e32 v150, s63
	v_cvt_f32_i32_e32 v151, s59
	v_cvt_f32_i32_e32 v152, s66
	s_add_u32 s18, s5, s4
	v_readlane_b32 s4, v241, 2
	s_addc_u32 s19, s4, 0
	v_readlane_b32 s4, v242, 62
	v_add3_u32 v8, s65, v158, v159
	v_mov_b32_e32 v57, v65
	v_readlane_b32 s5, v242, 63
	s_mov_b32 s29, 1
	s_or_b32 s49, s20, 24
	v_lshl_add_u64 v[58:59], s[4:5], 0, v[56:57]
	v_add_u32_e32 v57, s65, v1
	v_add_u32_e32 v123, s65, v2
	v_add_u32_e32 v157, s65, v3
	v_add_u32_e32 v162, s65, v4
	v_add_u32_e32 v163, s65, v5
	v_add_u32_e32 v164, s65, v6
	v_add_u32_e32 v165, s65, v7
	v_add_u32_e32 v166, s65, v0
	v_add_u32_e32 v167, v8, v67
	s_branch .LBB0_415

.LBB0_582:
	s_mov_b32 s0, s84
	s_waitcnt vmcnt(0)
	s_barrier
	v_readlane_b32 s100, v242, 48
	s_nop 3
	s_cmp_lg_u32 s100, 1
	s_cbranch_scc1 .Lxb_skipinv_4
	buffer_inv sc1
.Lxb_skipinv_4:
	s_and_saveexec_b64 s[4:5], s[76:77]
	s_cbranch_execz .LBB0_634
	v_readlane_b32 s1, v242, 32
	s_waitcnt vmcnt(0) expcnt(0) lgkmcnt(0)
	s_nop 0
	v_mov_b32_e32 v0, s1
	ds_read_b32 v2, v0
	v_readlane_b32 s1, v242, 33
	s_waitcnt lgkmcnt(0)
	v_cmp_ne_u32_e32 vcc, 0, v2
	v_mov_b32_e32 v0, s1
	ds_read_b32 v0, v0
	s_cbranch_vccnz .LBB0_598
	v_readlane_b32 s6, v243, 0
	v_readlane_b32 s7, v243, 1
	s_load_dwordx2 s[2:3], s[6:7], 0x4
	s_waitcnt lgkmcnt(0)
	s_mul_i32 s1, s2, s73
	s_mul_i32 s1, s1, s3
	s_mov_b32 s2, 1
	s_branch .LBB0_586

.LBB0_613:
	s_or_b64 exec, exec, s[8:9]
	s_waitcnt vmcnt(0)
	s_waitcnt vmcnt(0)

.LBB0_631:
	s_or_b64 exec, exec, s[6:7]
	s_mov_b64 s[6:7], exec
	v_mbcnt_lo_u32_b32 v0, s6, 0
	v_mbcnt_hi_u32_b32 v0, s7, v0
	v_cmp_eq_u32_e32 vcc, 0, v0
	s_waitcnt vmcnt(0)
	s_and_saveexec_b64 s[8:9], vcc
	s_cbranch_execz .LBB0_633
	s_add_i32 s78, s0, 0x900
	s_lshl_b64 s[0:1], s[78:79], 2
	s_add_u32 s0, s82, s0
	s_addc_u32 s1, s83, s1
	s_bcnt1_i32_b64 s2, s[6:7]
	v_mov_b32_e32 v0, s2
	global_atomic_add v65, v0, s[0:1]

.LBB0_634:
	s_or_b64 exec, exec, s[4:5]
	s_mov_b32 s0, s86
	s_waitcnt lgkmcnt(0)
	s_waitcnt vmcnt(0)
	s_barrier
	s_waitcnt vmcnt(9)
	v_mbcnt_lo_u32_b32 v0, -1, 0
	v_mbcnt_hi_u32_b32 v0, -1, v0
	s_nop 0
	v_lshl_add_u32 v64, s0, 6, v0
	s_mov_b32 s0, s79
	s_add_i32 s0, s0, 0x25f98
	v_mov_b32_e32 v0, s0
	ds_read_b64 v[0:1], v0
	v_readlane_b32 s0, v242, 2
	v_readlane_b32 s1, v242, 3
	s_andn2_b64 vcc, exec, s[0:1]
	s_waitcnt lgkmcnt(0)
	v_readfirstlane_b32 s8, v0
	v_readfirstlane_b32 s9, v1
	s_cbranch_vccnz .LBB0_641
	v_lshrrev_b32_e32 v1, 2, v64
	v_ashrrev_i32_e32 v0, 2, v64
	v_and_b32_e32 v1, 12, v1
	s_add_u32 s4, s8, 0x65800000
	v_and_or_b32 v0, v0, -16, v1
	s_addc_u32 s5, s9, 0
	v_ashrrev_i32_e32 v1, 31, v0
	s_add_u32 s6, s8, 0x69900000
	v_lshl_add_u64 v[0:1], v[0:1], 2, s[8:9]
	s_mov_b64 s[0:1], 0x6da00000
	s_addc_u32 s7, s9, 0
	v_lshl_add_u64 v[70:71], v[0:1], 0, s[0:1]
	s_mov_b32 s0, s74
	s_branch .LBB0_637

.LBB0_693:
	s_or_b64 exec, exec, s[4:5]
	s_mov_b32 s0, s86
	s_waitcnt lgkmcnt(0)
	s_waitcnt vmcnt(0)
	s_barrier
	v_mbcnt_lo_u32_b32 v0, -1, 0
	v_mbcnt_hi_u32_b32 v0, -1, v0
	s_mov_b32 s60, s79
	v_lshl_add_u32 v0, s0, 6, v0
	s_mov_b32 s0, s79
	s_add_i32 s0, s0, 0x25f98
	v_mov_b32_e32 v1, s0
	ds_read_b64 v[2:3], v1
	s_mov_b32 s2, s79
	s_add_i32 s2, s2, 0x25f60
	v_mov_b32_e32 v1, s2
	s_waitcnt lgkmcnt(0)
	v_readfirstlane_b32 s0, v2
	v_readfirstlane_b32 s1, v3
	ds_read_b64 v[2:3], v1
	s_mov_b32 s4, s79
	s_add_i32 s4, s4, 0x25f58
	v_mov_b32_e32 v1, s4
	s_waitcnt lgkmcnt(0)
	v_readfirstlane_b32 s2, v2
	v_readfirstlane_b32 s3, v3
	ds_read_b64 v[2:3], v1
	v_readfirstlane_b32 s70, v0
	s_ashr_i32 s18, s70, 6
	s_cmp_gt_i32 s18, 3
	s_cselect_b64 s[4:5], -1, 0
	s_waitcnt lgkmcnt(0)
	v_readfirstlane_b32 s6, v2
	v_readfirstlane_b32 s7, v3
	s_cmp_lt_i32 s18, 4
	s_cbranch_scc1 .LBB0_695
	s_setprio 1

.LBB0_753:
	s_setprio 0
	s_mov_b32 s2, s84
	s_waitcnt vmcnt(0)
	s_barrier
	v_readlane_b32 s100, v242, 48
	s_nop 3
	s_cmp_lg_u32 s100, 1
	s_cbranch_scc1 .Lxb_skipinv_6
	buffer_inv sc1

.LBB0_805:
	s_or_b64 exec, exec, s[0:1]
	v_readlane_b32 s2, v242, 55
	s_cmp_eq_u32 s2, 0
	s_mov_b64 s[6:7], 0
	s_cselect_b64 s[0:1], -1, 0
	s_cmp_lg_u32 s2, 0
	s_mov_b64 s[8:9], 0
	s_waitcnt lgkmcnt(0)
	s_waitcnt vmcnt(0)
	s_barrier
	v_readlane_b32 s3, v242, 56
	s_cbranch_scc0 .LBB0_899
	s_andn2_b64 vcc, exec, s[0:1]
	s_cbranch_vccz .LBB0_900

.LBB0_920:
	s_mov_b32 s2, s84
	s_waitcnt vmcnt(0)
	s_barrier
	v_readlane_b32 s100, v242, 48
	s_nop 3
	s_cmp_lg_u32 s100, 1
	s_cbranch_scc1 .Lxb_skipinv_7
	buffer_inv sc1

.LBB0_972:
	s_or_b64 exec, exec, s[0:1]
	s_mov_b32 s0, s86
	s_waitcnt lgkmcnt(0)
	s_waitcnt vmcnt(0)
	s_barrier
	s_waitcnt vmcnt(5)
	v_mbcnt_lo_u32_b32 v0, -1, 0
	v_mbcnt_hi_u32_b32 v0, -1, v0
	s_mov_b32 s2, s79
	v_lshl_add_u32 v131, s0, 6, v0
	s_mov_b32 s0, s79
	s_add_i32 s0, s0, 0x25f98
	v_mov_b32_e32 v0, s0
	ds_read_b64 v[0:1], v0
	v_readlane_b32 s4, v241, 10
	v_readlane_b32 s5, v241, 11
	s_and_b64 s[4:5], s[4:5], exec
	s_movk_i32 s1, 0x820
	s_cselect_b32 s22, 0x800, s1
	v_readlane_b32 s1, v243, 2
	v_readfirstlane_b32 s3, v131
	s_waitcnt lgkmcnt(0)
	v_readfirstlane_b32 s0, v0
	s_cmp_ge_i32 s1, s22
	v_readfirstlane_b32 s1, v1
	s_cbranch_scc1 .LBB0_989
	v_and_b32_e32 v132, 48, v131
	v_lshlrev_b32_e32 v64, 1, v132
	s_ashr_i32 s23, s3, 6
	v_lshl_add_u64 v[0:1], s[0:1], 0, v[64:65]
	s_mov_b64 s[4:5], 0x33400000
	s_add_u32 s8, s0, 0x6fe00000
	v_lshl_add_u64 v[134:135], v[0:1], 0, s[4:5]
	v_readlane_b32 s4, v242, 55
	s_addc_u32 s9, s1, 0
	v_and_b32_e32 v2, 63, v131
	v_readlane_b32 s5, v242, 56
	s_add_i32 s25, s2, 0x12000
	s_andn2_b32 s3, s3, 63
	s_lshl_b32 s24, s4, 16
	v_lshlrev_b32_e32 v0, 2, v2
	v_cmp_gt_u32_e64 s[4:5], 16, v2
	s_add_i32 s3, s25, s3
	v_lshlrev_b32_e32 v64, 4, v2
	v_lshrrev_b32_e32 v2, 2, v131
	v_mov_b32_e32 v133, v65
	v_xor_b32_e32 v148, 64, v0
	v_xor_b32_e32 v149, 0x80, v0
	v_add_u32_e32 v150, s3, v0
	v_lshlrev_b32_e32 v0, 2, v131
	v_and_b32_e32 v152, 12, v2
	v_lshl_add_u64 v[2:3], s[0:1], 0, v[64:65]
	s_mov_b64 s[10:11], 0x70000000
	s_waitcnt vmcnt(0)
	v_lshrrev_b32_e32 v4, 3, v131
	v_ashrrev_i32_e32 v1, 31, v0
	v_lshlrev_b32_e32 v151, 4, v131
	v_lshl_add_u64 v[136:137], v[2:3], 0, s[10:11]
	v_lshl_add_u64 v[2:3], s[0:1], 0, v[132:133]
	s_mov_b64 s[10:11], 0x3b600000
	v_lshlrev_b32_e32 v153, 2, v132
	v_and_b32_e32 v130, 15, v131
	v_cmp_gt_i32_e64 s[6:7], s87, v131
	s_add_i32 s26, s2, 0x10000
	s_add_i32 s27, s2, 0x11000
	v_lshl_add_u64 v[138:139], v[2:3], 0, s[10:11]
	v_add_u32_e32 v133, s2, v64
	v_or_b32_e32 v154, 0x100, v153
	v_or_b32_e32 v155, 0x200, v153
	v_or_b32_e32 v156, 0x300, v153
	v_or_b32_e32 v157, 0x400, v153
	v_or_b32_e32 v158, 0x500, v153
	v_or_b32_e32 v159, 0x600, v153
	v_or_b32_e32 v160, 0x700, v153
	v_or_b32_e32 v161, 0x800, v153
	v_or_b32_e32 v162, 0x900, v153
	v_or_b32_e32 v163, 0xa00, v153
	v_or_b32_e32 v164, 0xb00, v153
	v_or_b32_e32 v165, 0xc00, v153
	v_or_b32_e32 v166, 0xd00, v153
	v_or_b32_e32 v167, 0xe00, v153
	v_or_b32_e32 v168, 0xf00, v153
	v_and_or_b32 v169, v4, 8, v132
	v_add_u32_e32 v170, s2, v151
	s_mov_b32 s2, -1
	v_lshlrev_b64 v[140:141], 2, v[0:1]
	v_readlane_b32 s28, v243, 2
	s_branch .LBB0_975

.LBB0_997:
	s_mov_b32 s8, s84
	s_waitcnt vmcnt(0)
	s_barrier
	v_readlane_b32 s100, v242, 48
	s_nop 3
	s_cmp_lg_u32 s100, 1
	s_cbranch_scc1 .Lxb_skipinv_8
	buffer_inv sc1
.Lxb_skipinv_8:
	s_and_saveexec_b64 s[0:1], s[76:77]
	s_cbranch_execz .LBB0_1049
	v_readlane_b32 s2, v242, 32
	s_waitcnt vmcnt(0) expcnt(0) lgkmcnt(0)
	s_nop 0
	v_mov_b32_e32 v0, s2
	ds_read_b32 v2, v0
	v_readlane_b32 s2, v242, 33
	s_waitcnt lgkmcnt(0)
	v_cmp_ne_u32_e32 vcc, 0, v2
	v_mov_b32_e32 v0, s2
	ds_read_b32 v0, v0
	s_cbranch_vccnz .LBB0_1013
	v_readlane_b32 s4, v243, 0
	v_readlane_b32 s5, v243, 1
	s_load_dwordx2 s[2:3], s[4:5], 0x4
	s_mov_b32 s10, 1
	s_waitcnt lgkmcnt(0)
	s_mul_i32 s9, s2, s73
	s_mul_i32 s9, s9, s3
	s_branch .LBB0_1001

.LBB0_1046:
	s_or_b64 exec, exec, s[2:3]
	s_mov_b64 s[2:3], exec
	v_mbcnt_lo_u32_b32 v0, s2, 0
	v_mbcnt_hi_u32_b32 v0, s3, v0
	v_cmp_eq_u32_e32 vcc, 0, v0
	s_waitcnt vmcnt(0)
	s_and_saveexec_b64 s[4:5], vcc
	s_cbranch_execz .LBB0_1048
	s_add_i32 s78, s18, 0x900
	s_lshl_b64 s[6:7], s[78:79], 2
	s_add_u32 s6, s82, s6
	s_addc_u32 s7, s83, s7
	s_bcnt1_i32_b64 s2, s[2:3]
	v_mov_b32_e32 v0, s2
	global_atomic_add v65, v0, s[6:7]

.LBB0_1049:
	s_or_b64 exec, exec, s[0:1]
	s_mov_b32 s0, s86
	s_waitcnt lgkmcnt(0)
	s_waitcnt vmcnt(0)
	s_barrier
	v_mbcnt_lo_u32_b32 v0, -1, 0
	v_mbcnt_hi_u32_b32 v0, -1, v0
	s_mov_b32 s33, s79
	v_lshl_add_u32 v0, s0, 6, v0
	s_mov_b32 s0, s79
	s_add_i32 s0, s0, 0x25f98
	v_mov_b32_e32 v1, s0
	ds_read_b64 v[2:3], v1
	v_readlane_b32 s4, v241, 10
	v_readlane_b32 s5, v241, 11
	s_and_b64 s[4:5], s[4:5], exec
	s_cselect_b32 s1, 32, 64
	v_readfirstlane_b32 s2, v0
	s_waitcnt lgkmcnt(0)
	v_readfirstlane_b32 s0, v2
	v_writelane_b32 v241, s1, 16
	s_cmp_ge_i32 s74, s1
	v_readfirstlane_b32 s1, v3
	s_cbranch_scc1 .LBB0_1313
	s_ashr_i32 s2, s2, 6
	s_add_u32 s3, s0, 0x6fc00000
	v_writelane_b32 v241, s3, 4
	s_addc_u32 s3, s1, 0
	v_writelane_b32 v241, s3, 8
	s_add_u32 s3, s0, 0x6fe00000
	v_writelane_b32 v241, s3, 18
	s_addc_u32 s3, s1, 0
	s_add_u32 s68, s0, 0x6ff00000
	s_addc_u32 s69, s1, 0
	s_add_u32 s72, s0, 0x6ff44000
	s_addc_u32 s73, s1, 0
	s_add_u32 s76, s0, 0x70000000
	v_and_b32_e32 v62, 63, v0
	s_addc_u32 s77, s1, 0
	v_cmp_eq_u32_e64 s[0:1], 63, v62
	s_lshl_b32 s87, s2, 2
	v_add_u32_e32 v2, 0x400, v0
	v_writelane_b32 v240, s0, 1
	s_waitcnt vmcnt(0)
	v_add_u32_e32 v4, 0x600, v0
	v_add_u32_e32 v6, 0x800, v0
	v_writelane_b32 v240, s1, 2
	s_add_i32 s0, s33, s87
	v_writelane_b32 v240, s0, 3
	s_movk_i32 s0, 0xc0
	v_cmp_gt_i32_e64 s[0:1], s0, v0
	s_cmp_gt_i32 s2, 0
	v_add_u32_e32 v8, 0xa00, v0
	v_writelane_b32 v240, s0, 4
	v_add_u32_e32 v10, 0xc00, v0
	v_add_u32_e32 v12, 0xe00, v0
	v_writelane_b32 v240, s1, 5
	v_cmp_gt_u32_e64 s[0:1], 2, v62
	v_add_u32_e32 v14, 0x1000, v0
	v_add_u32_e32 v16, 0x1200, v0
	v_writelane_b32 v240, s0, 6
	v_add_u32_e32 v18, 0x1400, v0
	v_add_u32_e32 v20, 0x1600, v0
	v_writelane_b32 v240, s1, 7
	v_cmp_gt_u32_e64 s[0:1], 4, v62
	v_add_u32_e32 v22, 0x1800, v0
	v_add_u32_e32 v24, 0x1a00, v0
	v_writelane_b32 v240, s0, 8
	v_add_u32_e32 v26, 0x1c00, v0
	v_add_u32_e32 v28, 0x1e00, v0
	v_writelane_b32 v240, s1, 9
	v_cmp_gt_u32_e64 s[0:1], 8, v62
	v_add_u32_e32 v30, 0x2000, v0
	v_add_u32_e32 v32, 0x2200, v0
	v_writelane_b32 v240, s0, 10
	v_add_u32_e32 v34, 0x2400, v0
	v_add_u32_e32 v36, 0x2600, v0
	v_writelane_b32 v240, s1, 11
	v_cmp_gt_u32_e64 s[0:1], 16, v62
	v_add_u32_e32 v38, 0x2800, v0
	v_add_u32_e32 v40, 0x2a00, v0
	v_writelane_b32 v240, s0, 12
	v_add_u32_e32 v42, 0x2c00, v0
	v_add_u32_e32 v44, 0x2e00, v0
	v_writelane_b32 v240, s1, 13
	v_cmp_gt_u32_e64 s[0:1], 32, v62
	v_add_u32_e32 v46, 0x3000, v0
	v_add_u32_e32 v48, 0x3200, v0
	v_writelane_b32 v240, s0, 14
	v_add_u32_e32 v50, 0x3400, v0
	v_add_u32_e32 v52, 0x3600, v0
	v_writelane_b32 v240, s1, 15
	s_cselect_b64 s[0:1], -1, 0
	v_writelane_b32 v240, s0, 16
	s_cmp_gt_i32 s2, 1
	v_add_u32_e32 v54, 0x3800, v0
	v_writelane_b32 v240, s1, 17
	s_cselect_b64 s[0:1], -1, 0
	v_writelane_b32 v240, s0, 18
	s_cmp_gt_i32 s2, 2
	v_add_u32_e32 v56, 0x3a00, v0
	v_writelane_b32 v240, s1, 19
	s_cselect_b64 s[0:1], -1, 0
	v_writelane_b32 v240, s0, 20
	s_cmp_gt_i32 s2, 3
	v_add_u32_e32 v58, 0x3c00, v0
	v_writelane_b32 v240, s1, 21
	s_cselect_b64 s[0:1], -1, 0
	v_writelane_b32 v240, s0, 22
	s_cmp_gt_i32 s2, 4
	v_add_u32_e32 v60, 0x3e00, v0
	v_writelane_b32 v240, s1, 23
	s_cselect_b64 s[0:1], -1, 0
	v_writelane_b32 v240, s0, 24
	s_cmp_gt_i32 s2, 5
	v_lshlrev_b32_e32 v63, 2, v62
	v_writelane_b32 v240, s1, 25
	s_cselect_b64 s[0:1], -1, 0
	v_writelane_b32 v240, s0, 26
	s_cmp_gt_i32 s2, 6
	v_cmp_eq_u32_e32 vcc, 0, v62
	v_writelane_b32 v240, s1, 27
	s_cselect_b64 s[0:1], -1, 0
	v_writelane_b32 v240, s0, 28
	s_cmp_gt_i32 s2, 7
	v_add_u32_e32 v66, 0x1040, v0
	v_writelane_b32 v240, s1, 29
	s_cselect_b64 s[0:1], -1, 0
	v_ashrrev_i32_e32 v1, 31, v0
	v_add_u32_e32 v67, 0x200, v0
	v_ashrrev_i32_e32 v3, 31, v2
	v_ashrrev_i32_e32 v5, 31, v4
	v_ashrrev_i32_e32 v7, 31, v6
	v_ashrrev_i32_e32 v9, 31, v8
	v_ashrrev_i32_e32 v11, 31, v10
	v_ashrrev_i32_e32 v13, 31, v12
	v_ashrrev_i32_e32 v15, 31, v14
	v_ashrrev_i32_e32 v17, 31, v16
	v_ashrrev_i32_e32 v19, 31, v18
	v_ashrrev_i32_e32 v21, 31, v20
	v_ashrrev_i32_e32 v23, 31, v22
	v_ashrrev_i32_e32 v25, 31, v24
	v_ashrrev_i32_e32 v27, 31, v26
	v_ashrrev_i32_e32 v29, 31, v28
	v_ashrrev_i32_e32 v31, 31, v30
	v_ashrrev_i32_e32 v33, 31, v32
	v_ashrrev_i32_e32 v35, 31, v34
	v_ashrrev_i32_e32 v37, 31, v36
	v_ashrrev_i32_e32 v39, 31, v38
	v_ashrrev_i32_e32 v41, 31, v40
	v_ashrrev_i32_e32 v43, 31, v42
	v_ashrrev_i32_e32 v45, 31, v44
	v_ashrrev_i32_e32 v47, 31, v46
	v_ashrrev_i32_e32 v49, 31, v48
	v_ashrrev_i32_e32 v51, 31, v50
	v_ashrrev_i32_e32 v53, 31, v52
	v_ashrrev_i32_e32 v55, 31, v54
	v_ashrrev_i32_e32 v57, 31, v56
	v_ashrrev_i32_e32 v59, 31, v58
	v_ashrrev_i32_e32 v61, 31, v60
	v_add_u32_e32 v68, -4, v63
	v_add_u32_e32 v69, -8, v63
	v_add_u32_e32 v70, -16, v63
	v_subrev_u32_e32 v71, 32, v63
	v_subrev_u32_e32 v72, 64, v63
	v_add_u32_e32 v73, 0xffffff80, v63
	v_writelane_b32 v240, s0, 30
	s_mov_b32 s91, s74
	v_writelane_b32 v241, s3, 17
	v_writelane_b32 v240, s1, 31
	s_branch .LBB0_1052

.LBB0_1326:
	s_mov_b32 s8, s84
	s_waitcnt vmcnt(0)
	s_waitcnt vmcnt(63) expcnt(7) lgkmcnt(15)
	s_barrier
	v_readlane_b32 s100, v242, 48
	s_nop 3
	s_cmp_lg_u32 s100, 1
	s_cbranch_scc1 .Lxb_skipinv_9
	buffer_inv sc1

.LBB0_1378:
	s_or_b64 exec, exec, s[0:1]
	v_readlane_b32 s0, v241, 10
	v_readlane_b32 s1, v241, 11
	s_and_b64 s[0:1], s[0:1], exec
	s_cselect_b32 s33, 16, 17
	s_mov_b32 s4, s79
	s_mov_b32 s0, s86
	s_waitcnt lgkmcnt(0)
	s_waitcnt vmcnt(0)
	s_barrier
	v_mbcnt_lo_u32_b32 v0, -1, 0
	v_mbcnt_hi_u32_b32 v0, -1, v0
	s_lshl_b32 s34, s33, 4
	v_lshl_add_u32 v1, s0, 6, v0
	v_cvt_f32_u32_e32 v0, s34
	s_lshl_b32 s35, s33, 8
	s_cmp_lt_i32 s71, s35
	v_rcp_iflag_f32_e32 v0, v0
	s_cselect_b64 s[0:1], -1, 0
	s_cmp_ge_i32 s71, s35
	v_readfirstlane_b32 s5, v1
	s_cbranch_scc1 .LBB0_1383
	v_mul_f32_e32 v2, 0x4f7ffffe, v0
	v_cvt_u32_f32_e32 v2, v2
	s_sub_i32 s2, 0, s34
	v_readlane_b32 s7, v242, 31
	v_readfirstlane_b32 s3, v2
	s_mul_i32 s2, s2, s3
	s_mul_hi_u32 s2, s3, s2
	s_add_i32 s3, s3, s2
	s_mul_hi_u32 s2, s7, s3
	s_mul_i32 s3, s2, s34
	s_sub_i32 s3, s7, s3
	s_add_i32 s6, s2, 1
	s_sub_i32 s7, s3, s34
	s_cmp_ge_u32 s3, s34
	s_cselect_b32 s2, s6, s2
	s_cselect_b32 s3, s7, s3
	s_add_i32 s6, s2, 1
	s_cmp_ge_u32 s3, s34
	s_cselect_b32 s2, s6, s2
	v_readlane_b32 s3, v242, 30
	s_xor_b32 s2, s2, s3
	s_sub_i32 s6, s2, s3
	s_mul_i32 s2, s6, s34
	s_sub_i32 s7, s71, s2
	s_cmpk_gt_i32 s7, 0xff
	s_mul_i32 s8, s6, 17
	s_mov_b64 s[2:3], -1
	s_cbranch_scc0 .LBB0_1381
	s_lshr_b32 s2, s7, 4
	s_add_i32 s63, s2, s8
	s_lshl_b32 s2, s6, 4
	v_readlane_b32 s3, v242, 19
	s_or_b32 s18, s2, s3
	s_mov_b64 s[2:3], 0

.LBB0_1414:
	s_mov_b32 s10, s84
	s_waitcnt vmcnt(0)
	s_waitcnt vmcnt(0) lgkmcnt(0)
	s_barrier
	v_readlane_b32 s100, v242, 48
	s_nop 3
	s_cmp_lg_u32 s100, 1
	s_cbranch_scc1 .Lxb_skipinv_10
	buffer_inv sc1
.Lxb_skipinv_10:
	s_and_saveexec_b64 s[0:1], s[76:77]
	s_cbranch_execz .LBB0_1466
	v_readlane_b32 s2, v242, 32
	s_waitcnt vmcnt(0) expcnt(0) lgkmcnt(0)
	s_nop 0
	v_mov_b32_e32 v0, s2
	ds_read_b32 v2, v0
	v_readlane_b32 s2, v242, 33
	s_waitcnt lgkmcnt(0)
	v_cmp_ne_u32_e32 vcc, 0, v2
	v_mov_b32_e32 v0, s2
	ds_read_b32 v0, v0
	s_cbranch_vccnz .LBB0_1430
	v_readlane_b32 s4, v243, 0
	v_readlane_b32 s5, v243, 1
	s_load_dwordx2 s[2:3], s[4:5], 0x4
	s_mov_b32 s12, 1
	s_waitcnt lgkmcnt(0)
	s_mul_i32 s11, s2, s73
	s_mul_i32 s11, s11, s3
	s_branch .LBB0_1418

.LBB0_1463:
	s_or_b64 exec, exec, s[2:3]
	s_mov_b64 s[2:3], exec
	v_mbcnt_lo_u32_b32 v0, s2, 0
	v_mbcnt_hi_u32_b32 v0, s3, v0
	v_cmp_eq_u32_e32 vcc, 0, v0
	s_waitcnt vmcnt(0)
	s_and_saveexec_b64 s[4:5], vcc
	s_cbranch_execz .LBB0_1465
	s_add_i32 s78, s20, 0x900
	s_lshl_b64 s[8:9], s[78:79], 2
	s_add_u32 s8, s82, s8
	s_addc_u32 s9, s83, s9
	s_bcnt1_i32_b64 s2, s[2:3]
	v_mov_b32_e32 v0, s2
	global_atomic_add v65, v0, s[8:9]

.LBB0_1466:
	s_or_b64 exec, exec, s[0:1]
	s_mov_b32 s12, s79
	s_mov_b32 s0, s86
	s_waitcnt lgkmcnt(0)
	s_waitcnt vmcnt(0)
	s_barrier
	v_mbcnt_lo_u32_b32 v0, -1, 0
	v_mbcnt_hi_u32_b32 v0, -1, v0
	s_lshl_b32 s38, s33, 6
	v_lshl_add_u32 v0, s0, 6, v0
	s_cmp_ge_i32 s71, s38
	v_readfirstlane_b32 s10, v0
	s_cbranch_scc1 .LBB0_1490
	v_bfe_i32 v3, v0, 27, 1
	v_lshlrev_b32_e32 v1, 4, v0
	v_lshrrev_b32_e32 v3, 22, v3
	v_add_u32_e32 v3, v1, v3
	v_and_b32_e32 v3, 0xfffffc00, v3
	v_sub_u32_e32 v3, v1, v3
	v_ashrrev_i32_e32 v2, 31, v0
	v_lshrrev_b32_e32 v4, 4, v3
	v_lshrrev_b32_e32 v2, 26, v2
	v_bitop3_b32 v4, v4, v3, 32 bitop3:0x6c
	v_ashrrev_i32_e32 v3, 31, v3
	v_readlane_b32 s0, v242, 55
	v_add_u32_e32 v2, v0, v2
	v_lshrrev_b32_e32 v3, 26, v3
	v_readlane_b32 s1, v242, 56
	v_ashrrev_i32_e32 v2, 6, v2
	v_add_u32_e32 v3, v4, v3
	s_lshl_b64 s[0:1], s[0:1], 25
	v_readlane_b32 s2, v242, 51
	v_lshlrev_b32_e32 v5, 3, v2
	v_ashrrev_i32_e32 v3, 6, v3
	s_add_u32 s0, s2, s0
	v_readlane_b32 s2, v242, 52
	v_and_b32_e32 v5, -16, v5
	v_mul_i32_i24_e32 v6, 64, v3
	s_addc_u32 s1, s2, s1
	v_add_u32_e32 v5, v3, v5
	v_sub_u32_e32 v4, v4, v6
	s_add_u32 s39, s0, 0x23400000
	v_lshlrev_b32_e32 v2, 5, v2
	v_ashrrev_i16_sdwa v4, v201, sext(v4) dst_sel:DWORD dst_unused:UNUSED_PAD src0_sel:DWORD src1_sel:BYTE_0
	v_lshlrev_b32_e32 v6, 1, v5
	v_lshrrev_b32_e32 v7, 2, v5
	v_and_b32_e32 v3, 3, v3
	s_mov_b32 s0, 0x1fffe0
	v_and_b32_e32 v2, 32, v2
	v_bfe_i32 v4, v4, 0, 16
	v_and_b32_e32 v6, 24, v6
	v_and_b32_e32 v7, 4, v7
	v_and_or_b32 v3, v5, s0, v3
	v_or3_b32 v3, v3, v7, v6
	v_add_lshl_u32 v2, v2, v4, 1
	v_add_u32_e32 v1, 0x2000, v1
	v_lshl_add_u32 v211, v3, 11, v2
	v_lshl_add_u32 v212, v5, 11, v2
	v_ashrrev_i32_e32 v2, 31, v1
	v_lshrrev_b32_e32 v2, 22, v2
	v_add_u32_e32 v2, v1, v2
	v_ashrrev_i32_e32 v2, 10, v2
	v_mul_i32_i24_e32 v3, 0x400, v2
	v_sub_u32_e32 v1, v1, v3
	v_lshrrev_b32_e32 v3, 4, v1
	v_bitop3_b32 v1, v3, v1, 32 bitop3:0x6c
	v_ashrrev_i32_e32 v4, 31, v1
	v_lshrrev_b32_e32 v4, 26, v4
	v_lshlrev_b32_e32 v3, 3, v2
	v_add_u32_e32 v4, v1, v4
	v_and_b32_e32 v3, -16, v3
	v_ashrrev_i32_e32 v5, 6, v4
	v_add_u32_e32 v3, v5, v3
	v_and_b32_e32 v4, 0xc0, v4
	v_sub_u32_e32 v1, v1, v4
	v_lshlrev_b32_e32 v4, 1, v3
	v_lshrrev_b32_e32 v6, 2, v3
	v_and_b32_e32 v5, 3, v5
	s_addc_u32 s40, s1, 0
	v_and_b32_e32 v4, 24, v4
	v_and_b32_e32 v6, 4, v6
	v_and_or_b32 v5, v3, s0, v5
	s_lshl_b32 s33, s33, 2
	v_or3_b32 v4, v5, v6, v4
	v_cvt_f32_ubyte0_e32 v5, s33
	v_rcp_iflag_f32_e32 v5, v5
	v_lshlrev_b32_e32 v2, 5, v2
	v_ashrrev_i16_sdwa v1, v201, sext(v1) dst_sel:DWORD dst_unused:UNUSED_PAD src0_sel:DWORD src1_sel:BYTE_0
	v_and_b32_e32 v2, 32, v2
	v_bfe_i32 v1, v1, 0, 16
	v_add_lshl_u32 v1, v2, v1, 1
	v_lshl_add_u32 v213, v4, 11, v1
	v_lshl_add_u32 v214, v3, 11, v1
	v_mul_f32_e32 v1, 0x4f7ffffe, v5
	v_cvt_u32_f32_e32 v1, v1
	s_sub_i32 s0, 0, s33
	v_readlane_b32 s2, v242, 31
	s_ashr_i32 s14, s10, 6
	v_readfirstlane_b32 s41, v1
	s_mul_i32 s0, s0, s41
	s_mul_hi_u32 s0, s41, s0
	s_add_i32 s41, s41, s0
	s_mul_hi_u32 s0, s2, s41
	s_mul_i32 s1, s0, s33
	s_sub_i32 s1, s2, s1
	s_ashr_i32 s13, s10, 8
	s_lshl_b32 s11, s14, 10
	s_add_i32 s2, s0, 1
	s_sub_i32 s3, s1, s33
	s_cmp_ge_u32 s1, s33
	s_cselect_b32 s0, s2, s0
	s_cselect_b32 s1, s3, s1
	s_add_i32 s2, s0, 1
	s_cmp_ge_u32 s1, s33
	s_cselect_b32 s0, s2, s0
	v_readlane_b32 s1, v242, 30
	s_xor_b32 s0, s0, s1
	s_sub_i32 s0, s0, s1
	s_mul_i32 s1, s0, s33
	s_sub_i32 s1, s71, s1
	s_ashr_i32 s3, s1, 31
	s_lshr_b32 s3, s3, 30
	s_add_i32 s3, s1, s3
	s_mul_i32 s2, s0, 17
	s_ashr_i32 s4, s3, 2
	s_add_i32 s24, s4, s2
	s_and_b32 s2, s3, -4
	s_lshl_b32 s0, s0, 2
	s_sub_i32 s1, s1, s2
	s_add_i32 s22, s1, s0
	s_ashr_i32 s23, s22, 31
	s_lshl_b64 s[0:1], s[22:23], 19
	s_add_u32 s0, s39, s0
	s_addc_u32 s1, s40, s1
	s_ashr_i32 s25, s24, 31
	s_add_i32 s23, s12, 0x10000
	s_lshl_b64 s[2:3], s[24:25], 19
	s_add_i32 s25, s23, s11
	v_mov_b32_e32 v1, v211
	s_mov_b32 m0, s25
	s_add_i32 s42, s25, 0x2000
	global_load_lds_dwordx4 v1, s[0:1]
	v_mov_b32_e32 v1, v213
	s_add_u32 s4, s0, 0x40000
	s_mov_b32 m0, s42
	s_addc_u32 s5, s1, 0
	s_add_i32 s43, s12, 0x14000
	global_load_lds_dwordx4 v1, s[0:1]
	s_add_i32 s44, s43, s11
	v_mov_b32_e32 v1, v211
	s_mov_b32 m0, s44
	s_add_i32 s45, s44, 0x2000
	global_load_lds_dwordx4 v1, s[4:5]
	v_mov_b32_e32 v1, v213
	s_mov_b32 m0, s45
	s_add_u32 s2, s6, s2
	global_load_lds_dwordx4 v1, s[4:5]
	s_addc_u32 s3, s7, s3
	s_add_i32 s46, s12, s11
	v_mov_b32_e32 v1, v212
	s_mov_b32 m0, s46
	s_add_i32 s47, s46, 0x2000
	global_load_lds_dwordx4 v1, s[2:3]
	v_mov_b32_e32 v1, v214
	s_mov_b32 m0, s47
	s_add_u32 s4, s2, 0x40000
	global_load_lds_dwordx4 v1, s[2:3]
	s_addc_u32 s5, s3, 0
	s_add_i32 s48, s46, 0x4000
	v_mov_b32_e32 v1, v212
	s_mov_b32 m0, s48
	s_add_i32 s49, s46, 0x6000
	global_load_lds_dwordx4 v1, s[4:5]
	v_mov_b32_e32 v1, v214
	s_mov_b32 m0, s49
	s_cmp_eq_u32 s13, 1
	global_load_lds_dwordx4 v1, s[4:5]
	s_cselect_b64 s[4:5], -1, 0
	s_cmp_lg_u32 s13, 1
	s_cbranch_scc1 .LBB0_1469
	s_barrier

.LBB0_1515:
	s_mov_b32 s8, s84
	s_waitcnt vmcnt(0)
	s_waitcnt vmcnt(0) lgkmcnt(0)
	s_barrier
	v_readlane_b32 s100, v242, 48
	s_nop 3
	s_cmp_lg_u32 s100, 1
	s_cbranch_scc1 .Lxb_skipinv_11
	buffer_inv sc1
.Lxb_skipinv_11:
	s_and_saveexec_b64 s[0:1], s[76:77]
	s_cbranch_execnz .LBB0_1516
	s_getpc_b64 s[98:99]

.LBB0_1564:
	s_or_b64 exec, exec, s[2:3]
	s_mov_b64 s[2:3], exec
	v_mbcnt_lo_u32_b32 v0, s2, 0
	v_mbcnt_hi_u32_b32 v0, s3, v0
	v_cmp_eq_u32_e32 vcc, 0, v0
	s_waitcnt vmcnt(0)
	s_and_saveexec_b64 s[4:5], vcc
	s_cbranch_execnz .LBB0_1565
	s_getpc_b64 s[98:99]

	.amdhsa_kernel _Z8mega_fwd4Args
		.amdhsa_group_segment_fixed_size 0
		.amdhsa_private_segment_fixed_size 0
		.amdhsa_kernarg_size 416
		.amdhsa_user_sgpr_count 2
		.amdhsa_user_sgpr_dispatch_ptr 0
		.amdhsa_user_sgpr_queue_ptr 0
		.amdhsa_user_sgpr_kernarg_segment_ptr 1
		.amdhsa_user_sgpr_dispatch_id 0
		.amdhsa_user_sgpr_kernarg_preload_length 0
		.amdhsa_user_sgpr_kernarg_preload_offset 0
		.amdhsa_user_sgpr_private_segment_size 0
		.amdhsa_uses_dynamic_stack 0
		.amdhsa_enable_private_segment 0
		.amdhsa_system_sgpr_workgroup_id_x 1
		.amdhsa_system_sgpr_workgroup_id_y 0
		.amdhsa_system_sgpr_workgroup_id_z 0
		.amdhsa_system_sgpr_workgroup_info 0
		.amdhsa_system_vgpr_workitem_id 0
		.amdhsa_next_free_vgpr 244
		.amdhsa_next_free_sgpr 102
		.amdhsa_accum_offset 244
		.amdhsa_reserve_vcc 1
		.amdhsa_float_round_mode_32 0
		.amdhsa_float_round_mode_16_64 0
		.amdhsa_float_denorm_mode_32 3
		.amdhsa_float_denorm_mode_16_64 3
		.amdhsa_dx10_clamp 1
		.amdhsa_ieee_mode 1
		.amdhsa_fp16_overflow 0
		.amdhsa_tg_split 0
		.amdhsa_exception_fp_ieee_invalid_op 0
		.amdhsa_exception_fp_denorm_src 0
		.amdhsa_exception_fp_ieee_div_zero 0
		.amdhsa_exception_fp_ieee_overflow 0
		.amdhsa_exception_fp_ieee_underflow 0
		.amdhsa_exception_fp_ieee_inexact 0
		.amdhsa_exception_int_div_zero 0
	.end_amdhsa_kernel

amdhsa.kernels:
  - .agpr_count:     0
    .args:
      - .offset:         0
        .size:           160
        .value_kind:     by_value
      - .offset:         160
        .size:           4
        .value_kind:     hidden_block_count_x
      - .offset:         164
        .size:           4
        .value_kind:     hidden_block_count_y
      - .offset:         168
        .size:           4
        .value_kind:     hidden_block_count_z
      - .offset:         172
        .size:           2
        .value_kind:     hidden_group_size_x
      - .offset:         174
        .size:           2
        .value_kind:     hidden_group_size_y
      - .offset:         176
        .size:           2
        .value_kind:     hidden_group_size_z
      - .offset:         178
        .size:           2
        .value_kind:     hidden_remainder_x
      - .offset:         180
        .size:           2
        .value_kind:     hidden_remainder_y
      - .offset:         182
        .size:           2
        .value_kind:     hidden_remainder_z
      - .offset:         200
        .size:           8
        .value_kind:     hidden_global_offset_x
      - .offset:         208
        .size:           8
        .value_kind:     hidden_global_offset_y
      - .offset:         216
        .size:           8
        .value_kind:     hidden_global_offset_z
      - .offset:         224
        .size:           2
        .value_kind:     hidden_grid_dims
      - .offset:         280
        .size:           4
        .value_kind:     hidden_dynamic_lds_size
    .group_segment_fixed_size: 0
    .kernarg_segment_align: 8
    .kernarg_segment_size: 416
    .language:       OpenCL C
    .language_version:
      - 2
      - 0
    .max_flat_workgroup_size: 512
    .name:           _Z8mega_fwd4Args
    .private_segment_fixed_size: 0
    .sgpr_count:     108
    .sgpr_spill_count: 333
    .symbol:         _Z8mega_fwd4Args.kd
    .uniform_work_group_size: 1
    .uses_dynamic_stack: false
    .vgpr_count:     244
    .vgpr_spill_count: 0
    .wavefront_size: 64
